# fp8 kernels: descriptor and address setup of every stage hoisted out of the load segments into the previous MFMA run (28 scalar ops per iteration)
# speedup vs baseline: 1.0077x; 1.0077x over previous
.LBB3_4:
	ds_read_b128 v[2:5], v203
	ds_read_b128 v[10:13], v203 offset:2048
	ds_read_b128 v[6:9], v204
	ds_read_b128 v[14:17], v204 offset:2048
	s_mov_b32 m0, s46
	ds_read_b128 v[58:61], v200
	ds_read_b128 v[50:53], v200 offset:2048
	ds_read_b128 v[62:65], v201
	ds_read_b128 v[54:57], v201 offset:2048
	ds_read_b128 v[42:45], v200 offset:4096
	ds_read_b128 v[34:37], v200 offset:6144
	ds_read_b128 v[46:49], v201 offset:4096
	ds_read_b128 v[38:41], v201 offset:6144
	s_waitcnt vmcnt(8)
	buffer_load_dwordx4 v1, s[12:15], 0 offen lds
	s_mov_b32 m0, s47
	s_nop 0
	buffer_load_dwordx4 v195, s[12:15], 0 offen lds
	s_waitcnt lgkmcnt(8)
	s_barrier
	s_waitcnt lgkmcnt(0)
	s_setprio 1
	v_mfma_f32_16x16x128_f8f6f4 v[190:193], v[2:9], v[58:65], v[190:193]
	s_and_b32 s21, s53, 0xffff
	s_mov_b32 s22, s14
	s_mov_b32 s23, s15
	v_mfma_f32_16x16x128_f8f6f4 v[186:189], v[10:17], v[58:65], v[186:189]
	v_mfma_f32_16x16x128_f8f6f4 v[174:177], v[2:9], v[50:57], v[174:177]
	v_mfma_f32_16x16x128_f8f6f4 v[170:173], v[10:17], v[50:57], v[170:173]
	v_mfma_f32_16x16x128_f8f6f4 v[158:161], v[2:9], v[42:49], v[158:161]
	v_mfma_f32_16x16x128_f8f6f4 v[154:157], v[10:17], v[42:49], v[154:157]
	v_mfma_f32_16x16x128_f8f6f4 v[142:145], v[2:9], v[34:41], v[142:145]
	v_mfma_f32_16x16x128_f8f6f4 v[138:141], v[10:17], v[34:41], v[138:141]
	s_setprio 0
	s_barrier
	ds_read_b128 v[26:29], v205
	ds_read_b128 v[18:21], v205 offset:2048
	ds_read_b128 v[30:33], v206
	ds_read_b128 v[22:25], v206 offset:2048
	s_waitcnt vmcnt(8)
	s_and_b64 vcc, exec, s[18:19]
	s_cbranch_vccnz .LBB3_6
	s_mov_b32 m0, s33
	s_nop 0
	buffer_load_dwordx4 v194, s[20:23], 0 offen lds
	s_mov_b32 m0, s34
	s_nop 0
	buffer_load_dwordx4 v196, s[20:23], 0 offen lds
.LBB3_6:
	s_barrier
	s_waitcnt lgkmcnt(0)
	s_setprio 1
	v_mfma_f32_16x16x128_f8f6f4 v[182:185], v[26:33], v[58:65], v[182:185]
	s_add_u32 s12, s54, 0x100
	s_addc_u32 s21, s55, 0
	s_and_b32 s13, s21, 0xffff
	v_mfma_f32_16x16x128_f8f6f4 v[178:181], v[18:25], v[58:65], v[178:181]
	v_mfma_f32_16x16x128_f8f6f4 v[166:169], v[26:33], v[50:57], v[166:169]
	v_mfma_f32_16x16x128_f8f6f4 v[162:165], v[18:25], v[50:57], v[162:165]
	v_mfma_f32_16x16x128_f8f6f4 v[150:153], v[26:33], v[42:49], v[150:153]
	v_mfma_f32_16x16x128_f8f6f4 v[146:149], v[18:25], v[42:49], v[146:149]
	v_mfma_f32_16x16x128_f8f6f4 v[134:137], v[26:33], v[34:41], v[134:137]
	v_mfma_f32_16x16x128_f8f6f4 v[130:133], v[18:25], v[34:41], v[130:133]
	s_setprio 0
	s_barrier
	ds_read_b128 v[58:61], v200 offset:16384
	ds_read_b128 v[50:53], v200 offset:18432
	ds_read_b128 v[62:65], v201 offset:16384
	ds_read_b128 v[54:57], v201 offset:18432
	ds_read_b128 v[42:45], v200 offset:20480
	ds_read_b128 v[34:37], v200 offset:22528
	ds_read_b128 v[46:49], v201 offset:20480
	ds_read_b128 v[38:41], v201 offset:22528
	v_cndmask_b32_e64 v207, 0, 1, s[26:27]
	v_cmp_ne_u32_e64 s[0:1], 1, v207
	s_andn2_b64 vcc, exec, s[26:27]
	s_cbranch_vccnz .LBB3_8
	s_mov_b32 m0, s31
	s_nop 0
	buffer_load_dwordx4 v1, s[12:15], 0 offen lds
	s_mov_b32 m0, s35
	s_nop 0
	buffer_load_dwordx4 v195, s[12:15], 0 offen lds
.LBB3_8:
	s_barrier
	s_waitcnt lgkmcnt(0)
	s_setprio 1
	v_mfma_f32_16x16x128_f8f6f4 v[126:129], v[2:9], v[58:65], v[126:129]
	s_add_u32 s56, s51, 0x10100
	s_addc_u32 s13, s52, 0
	s_and_b32 s57, s13, 0xffff
	s_mov_b32 s58, s14
	v_mfma_f32_16x16x128_f8f6f4 v[122:125], v[10:17], v[58:65], v[122:125]
	s_mov_b32 s59, s15
	v_mfma_f32_16x16x128_f8f6f4 v[110:113], v[2:9], v[50:57], v[110:113]
	v_mfma_f32_16x16x128_f8f6f4 v[106:109], v[10:17], v[50:57], v[106:109]
	v_mfma_f32_16x16x128_f8f6f4 v[94:97], v[2:9], v[42:49], v[94:97]
	v_mfma_f32_16x16x128_f8f6f4 v[90:93], v[10:17], v[42:49], v[90:93]
	v_mfma_f32_16x16x128_f8f6f4 v[78:81], v[2:9], v[34:41], v[78:81]
	v_mfma_f32_16x16x128_f8f6f4 v[74:77], v[10:17], v[34:41], v[74:77]
	s_setprio 0
	s_barrier
	s_and_b64 vcc, exec, s[0:1]
	s_mov_b64 s[22:23], -1
	s_cbranch_vccnz .LBB3_10
	s_mov_b32 m0, s17
	s_nop 0
	buffer_load_dwordx4 v194, s[56:59], 0 offen lds
	s_mov_b32 m0, s36
	s_mov_b64 s[22:23], 0
	buffer_load_dwordx4 v196, s[56:59], 0 offen lds
	s_waitcnt vmcnt(10)

.LBB3_12:
	s_barrier
	s_setprio 1
	v_mfma_f32_16x16x128_f8f6f4 v[118:121], v[26:33], v[58:65], v[118:121]
	s_add_i32 s13, 0, 0x18000
	v_add_u32_e32 v2, s13, v198
	v_add_u32_e32 v6, s13, v199
	v_mfma_f32_16x16x128_f8f6f4 v[114:117], v[18:25], v[58:65], v[114:117]
	s_add_u32 s56, s54, 0x100100
	s_addc_u32 s13, s55, 0
	s_and_b32 s57, s13, 0xffff
	s_mov_b32 s58, s14
	v_mfma_f32_16x16x128_f8f6f4 v[102:105], v[26:33], v[50:57], v[102:105]
	s_mov_b32 s59, s15
	v_mfma_f32_16x16x128_f8f6f4 v[98:101], v[18:25], v[50:57], v[98:101]
	v_mfma_f32_16x16x128_f8f6f4 v[86:89], v[26:33], v[42:49], v[86:89]
	v_mfma_f32_16x16x128_f8f6f4 v[82:85], v[18:25], v[42:49], v[82:85]
	v_mfma_f32_16x16x128_f8f6f4 v[70:73], v[26:33], v[34:41], v[70:73]
	v_mfma_f32_16x16x128_f8f6f4 v[66:69], v[18:25], v[34:41], v[66:69]
	s_setprio 0
	s_barrier
	ds_read_b128 v[10:13], v2
	ds_read_b128 v[2:5], v2 offset:2048
	ds_read_b128 v[14:17], v6
	ds_read_b128 v[6:9], v6 offset:2048
	ds_read_b128 v[58:61], v200 offset:32768
	ds_read_b128 v[50:53], v200 offset:34816
	ds_read_b128 v[62:65], v201 offset:32768
	ds_read_b128 v[54:57], v201 offset:34816
	ds_read_b128 v[42:45], v200 offset:36864
	ds_read_b128 v[34:37], v200 offset:38912
	ds_read_b128 v[46:49], v201 offset:36864
	ds_read_b128 v[38:41], v201 offset:38912
	s_waitcnt vmcnt(8)
	s_and_b64 vcc, exec, s[0:1]
	s_cbranch_vccnz .LBB3_14
	s_mov_b32 m0, s37
	s_nop 0
	buffer_load_dwordx4 v1, s[56:59], 0 offen lds
	s_mov_b32 m0, s38
	s_nop 0
	buffer_load_dwordx4 v195, s[56:59], 0 offen lds
.LBB3_14:
	s_waitcnt lgkmcnt(8)
	s_barrier
	s_waitcnt lgkmcnt(0)
	s_setprio 1
	v_mfma_f32_16x16x128_f8f6f4 v[190:193], v[10:17], v[58:65], v[190:193]
	s_and_b64 s[22:23], exec, s[18:19]
	s_cselect_b32 s20, s8, s20
	s_cselect_b32 s13, s25, s53
	v_mfma_f32_16x16x128_f8f6f4 v[186:189], v[2:9], v[58:65], v[186:189]
	s_add_u32 s56, s20, 0x80
	s_addc_u32 s13, s13, 0
	s_and_b32 s57, s13, 0xffff
	s_mov_b32 s58, s14
	v_mfma_f32_16x16x128_f8f6f4 v[174:177], v[10:17], v[50:57], v[174:177]
	s_mov_b32 s59, s15
	v_mfma_f32_16x16x128_f8f6f4 v[170:173], v[2:9], v[50:57], v[170:173]
	v_mfma_f32_16x16x128_f8f6f4 v[158:161], v[10:17], v[42:49], v[158:161]
	v_mfma_f32_16x16x128_f8f6f4 v[154:157], v[2:9], v[42:49], v[154:157]
	v_mfma_f32_16x16x128_f8f6f4 v[142:145], v[10:17], v[34:41], v[142:145]
	v_mfma_f32_16x16x128_f8f6f4 v[138:141], v[2:9], v[34:41], v[138:141]
	s_setprio 0
	s_barrier
	ds_read_b128 v[26:29], v210
	ds_read_b128 v[18:21], v210 offset:2048
	ds_read_b128 v[30:33], v211
	ds_read_b128 v[22:25], v211 offset:2048
	s_waitcnt vmcnt(8)
	s_and_b64 vcc, exec, s[0:1]
	s_cbranch_vccnz .LBB3_16
	s_mov_b32 m0, s40
	s_nop 0
	buffer_load_dwordx4 v194, s[56:59], 0 offen lds
	s_mov_b32 m0, s41
	s_nop 0
	buffer_load_dwordx4 v196, s[56:59], 0 offen lds
.LBB3_16:
	s_barrier
	s_waitcnt lgkmcnt(0)
	s_setprio 1
	v_mfma_f32_16x16x128_f8f6f4 v[182:185], v[26:33], v[58:65], v[182:185]
	s_and_b64 s[18:19], exec, s[18:19]
	s_cselect_b32 s12, s16, s12
	s_cselect_b32 s13, s9, s21
	v_mfma_f32_16x16x128_f8f6f4 v[178:181], v[18:25], v[58:65], v[178:181]
	s_add_u32 s12, s12, 0x80
	s_addc_u32 s13, s13, 0
	s_and_b32 s13, s13, 0xffff
	v_mfma_f32_16x16x128_f8f6f4 v[166:169], v[26:33], v[50:57], v[166:169]
	v_mfma_f32_16x16x128_f8f6f4 v[162:165], v[18:25], v[50:57], v[162:165]
	v_mfma_f32_16x16x128_f8f6f4 v[150:153], v[26:33], v[42:49], v[150:153]
	v_mfma_f32_16x16x128_f8f6f4 v[146:149], v[18:25], v[42:49], v[146:149]
	v_mfma_f32_16x16x128_f8f6f4 v[134:137], v[26:33], v[34:41], v[134:137]
	v_mfma_f32_16x16x128_f8f6f4 v[130:133], v[18:25], v[34:41], v[130:133]
	s_setprio 0
	s_barrier
	ds_read_b128 v[58:61], v200 offset:49152
	ds_read_b128 v[50:53], v200 offset:51200
	ds_read_b128 v[62:65], v201 offset:49152
	ds_read_b128 v[54:57], v201 offset:51200
	ds_read_b128 v[42:45], v200 offset:53248
	ds_read_b128 v[34:37], v200 offset:55296
	ds_read_b128 v[46:49], v201 offset:53248
	ds_read_b128 v[38:41], v201 offset:55296
	s_and_b64 vcc, exec, s[0:1]
	s_cbranch_vccnz .LBB3_18
	s_mov_b32 m0, s42
	s_nop 0
	buffer_load_dwordx4 v1, s[12:15], 0 offen lds
	s_mov_b32 m0, s43
	s_nop 0
	buffer_load_dwordx4 v195, s[12:15], 0 offen lds

.LBB4_14:
	ds_read_b128 v[0:3], v202
	ds_read_b128 v[8:11], v202 offset:2048
	ds_read_b128 v[4:7], v203
	ds_read_b128 v[12:15], v203 offset:2048
	s_mov_b32 m0, s42
	ds_read_b128 v[56:59], v200
	ds_read_b128 v[48:51], v200 offset:2048
	ds_read_b128 v[60:63], v201
	ds_read_b128 v[52:55], v201 offset:2048
	ds_read_b128 v[40:43], v200 offset:4096
	ds_read_b128 v[32:35], v200 offset:6144
	ds_read_b128 v[44:47], v201 offset:4096
	ds_read_b128 v[36:39], v201 offset:6144
	s_waitcnt vmcnt(8)
	buffer_load_dwordx4 v192, s[12:15], 0 offen lds
	s_mov_b32 m0, s43
	s_nop 0
	buffer_load_dwordx4 v194, s[12:15], 0 offen lds
	s_waitcnt lgkmcnt(8)
	s_barrier
	s_waitcnt lgkmcnt(0)
	s_setprio 1
	v_mfma_f32_16x16x128_f8f6f4 v[188:191], v[0:7], v[56:63], v[188:191]
	s_and_b32 s21, s48, 0xffff
	s_mov_b32 s22, s14
	s_mov_b32 s23, s15
	v_mfma_f32_16x16x128_f8f6f4 v[184:187], v[8:15], v[56:63], v[184:187]
	v_mfma_f32_16x16x128_f8f6f4 v[172:175], v[0:7], v[48:55], v[172:175]
	v_mfma_f32_16x16x128_f8f6f4 v[168:171], v[8:15], v[48:55], v[168:171]
	v_mfma_f32_16x16x128_f8f6f4 v[156:159], v[0:7], v[40:47], v[156:159]
	v_mfma_f32_16x16x128_f8f6f4 v[152:155], v[8:15], v[40:47], v[152:155]
	v_mfma_f32_16x16x128_f8f6f4 v[140:143], v[0:7], v[32:39], v[140:143]
	v_mfma_f32_16x16x128_f8f6f4 v[136:139], v[8:15], v[32:39], v[136:139]
	s_setprio 0
	s_barrier
	ds_read_b128 v[24:27], v204
	ds_read_b128 v[16:19], v204 offset:2048
	ds_read_b128 v[28:31], v205
	ds_read_b128 v[20:23], v205 offset:2048
	s_waitcnt vmcnt(8)
	s_and_b64 vcc, exec, s[18:19]
	s_cbranch_vccnz .LBB4_16
	s_mov_b32 m0, s28
	s_nop 0
	buffer_load_dwordx4 v193, s[20:23], 0 offen lds
	s_mov_b32 m0, s29
	s_nop 0
	buffer_load_dwordx4 v195, s[20:23], 0 offen lds
.LBB4_16:
	s_barrier
	s_waitcnt lgkmcnt(0)
	s_setprio 1
	v_mfma_f32_16x16x128_f8f6f4 v[180:183], v[24:31], v[56:63], v[180:183]
	s_add_u32 s12, s49, 0x100
	s_addc_u32 s21, s50, 0
	s_and_b32 s13, s21, 0xffff
	v_mfma_f32_16x16x128_f8f6f4 v[176:179], v[16:23], v[56:63], v[176:179]
	v_mfma_f32_16x16x128_f8f6f4 v[164:167], v[24:31], v[48:55], v[164:167]
	v_mfma_f32_16x16x128_f8f6f4 v[160:163], v[16:23], v[48:55], v[160:163]
	v_mfma_f32_16x16x128_f8f6f4 v[148:151], v[24:31], v[40:47], v[148:151]
	v_mfma_f32_16x16x128_f8f6f4 v[144:147], v[16:23], v[40:47], v[144:147]
	v_mfma_f32_16x16x128_f8f6f4 v[132:135], v[24:31], v[32:39], v[132:135]
	v_mfma_f32_16x16x128_f8f6f4 v[128:131], v[16:23], v[32:39], v[128:131]
	s_setprio 0
	s_barrier
	ds_read_b128 v[56:59], v200 offset:16384
	ds_read_b128 v[48:51], v200 offset:18432
	ds_read_b128 v[60:63], v201 offset:16384
	ds_read_b128 v[52:55], v201 offset:18432
	ds_read_b128 v[40:43], v200 offset:20480
	ds_read_b128 v[32:35], v200 offset:22528
	ds_read_b128 v[44:47], v201 offset:20480
	ds_read_b128 v[36:39], v201 offset:22528
	v_cndmask_b32_e64 v206, 0, 1, s[24:25]
	v_cmp_ne_u32_e64 s[0:1], 1, v206
	s_andn2_b64 vcc, exec, s[24:25]
	s_cbranch_vccnz .LBB4_18
	s_mov_b32 m0, s7
	s_nop 0
	buffer_load_dwordx4 v192, s[12:15], 0 offen lds
	s_mov_b32 m0, s30
	s_nop 0
	buffer_load_dwordx4 v194, s[12:15], 0 offen lds
.LBB4_18:
	s_barrier
	s_waitcnt lgkmcnt(0)
	s_setprio 1
	v_mfma_f32_16x16x128_f8f6f4 v[124:127], v[0:7], v[56:63], v[124:127]
	s_add_u32 s52, s46, 0x4100
	s_addc_u32 s13, s47, 0
	s_and_b32 s53, s13, 0xffff
	s_mov_b32 s54, s14
	v_mfma_f32_16x16x128_f8f6f4 v[120:123], v[8:15], v[56:63], v[120:123]
	s_mov_b32 s55, s15
	v_mfma_f32_16x16x128_f8f6f4 v[108:111], v[0:7], v[48:55], v[108:111]
	v_mfma_f32_16x16x128_f8f6f4 v[104:107], v[8:15], v[48:55], v[104:107]
	v_mfma_f32_16x16x128_f8f6f4 v[92:95], v[0:7], v[40:47], v[92:95]
	v_mfma_f32_16x16x128_f8f6f4 v[88:91], v[8:15], v[40:47], v[88:91]
	v_mfma_f32_16x16x128_f8f6f4 v[76:79], v[0:7], v[32:39], v[76:79]
	v_mfma_f32_16x16x128_f8f6f4 v[72:75], v[8:15], v[32:39], v[72:75]
	s_setprio 0
	s_barrier
	s_and_b64 vcc, exec, s[0:1]
	s_mov_b64 s[22:23], -1
	s_cbranch_vccnz .LBB4_20
	s_mov_b32 m0, s17
	s_nop 0
	buffer_load_dwordx4 v193, s[52:55], 0 offen lds
	s_mov_b32 m0, s31
	s_mov_b64 s[22:23], 0
	buffer_load_dwordx4 v195, s[52:55], 0 offen lds
	s_waitcnt vmcnt(10)

.LBB4_22:
	s_barrier
	s_setprio 1
	v_mfma_f32_16x16x128_f8f6f4 v[116:119], v[24:31], v[56:63], v[116:119]
	v_add_u32_e32 v0, s45, v198
	v_add_u32_e32 v4, s45, v199
	s_add_u32 s52, s49, 0x40100
	s_addc_u32 s13, s50, 0
	v_mfma_f32_16x16x128_f8f6f4 v[112:115], v[16:23], v[56:63], v[112:115]
	s_and_b32 s53, s13, 0xffff
	s_mov_b32 s54, s14
	s_mov_b32 s55, s15
	v_mfma_f32_16x16x128_f8f6f4 v[100:103], v[24:31], v[48:55], v[100:103]
	v_mfma_f32_16x16x128_f8f6f4 v[96:99], v[16:23], v[48:55], v[96:99]
	v_mfma_f32_16x16x128_f8f6f4 v[84:87], v[24:31], v[40:47], v[84:87]
	v_mfma_f32_16x16x128_f8f6f4 v[80:83], v[16:23], v[40:47], v[80:83]
	v_mfma_f32_16x16x128_f8f6f4 v[68:71], v[24:31], v[32:39], v[68:71]
	v_mfma_f32_16x16x128_f8f6f4 v[64:67], v[16:23], v[32:39], v[64:67]
	s_setprio 0
	s_barrier
	ds_read_b128 v[8:11], v0
	ds_read_b128 v[0:3], v0 offset:2048
	ds_read_b128 v[12:15], v4
	ds_read_b128 v[4:7], v4 offset:2048
	ds_read_b128 v[56:59], v200 offset:32768
	ds_read_b128 v[48:51], v200 offset:34816
	ds_read_b128 v[60:63], v201 offset:32768
	ds_read_b128 v[52:55], v201 offset:34816
	ds_read_b128 v[40:43], v200 offset:36864
	ds_read_b128 v[32:35], v200 offset:38912
	ds_read_b128 v[44:47], v201 offset:36864
	ds_read_b128 v[36:39], v201 offset:38912
	s_waitcnt vmcnt(8)
	s_and_b64 vcc, exec, s[0:1]
	s_cbranch_vccnz .LBB4_24
	s_mov_b32 m0, s34
	s_nop 0
	buffer_load_dwordx4 v192, s[52:55], 0 offen lds
	s_mov_b32 m0, s35
	s_nop 0
	buffer_load_dwordx4 v194, s[52:55], 0 offen lds
.LBB4_24:
	s_waitcnt lgkmcnt(8)
	s_barrier
	s_waitcnt lgkmcnt(0)
	s_setprio 1
	v_mfma_f32_16x16x128_f8f6f4 v[188:191], v[8:15], v[56:63], v[188:191]
	s_and_b64 s[22:23], exec, s[18:19]
	s_cselect_b32 s20, s8, s20
	s_cselect_b32 s13, s3, s48
	v_mfma_f32_16x16x128_f8f6f4 v[184:187], v[0:7], v[56:63], v[184:187]
	s_add_u32 s48, s20, 0x80
	s_addc_u32 s13, s13, 0
	s_and_b32 s49, s13, 0xffff
	s_mov_b32 s50, s14
	v_mfma_f32_16x16x128_f8f6f4 v[172:175], v[8:15], v[48:55], v[172:175]
	s_mov_b32 s51, s15
	v_mfma_f32_16x16x128_f8f6f4 v[168:171], v[0:7], v[48:55], v[168:171]
	v_mfma_f32_16x16x128_f8f6f4 v[156:159], v[8:15], v[40:47], v[156:159]
	v_mfma_f32_16x16x128_f8f6f4 v[152:155], v[0:7], v[40:47], v[152:155]
	v_mfma_f32_16x16x128_f8f6f4 v[140:143], v[8:15], v[32:39], v[140:143]
	v_mfma_f32_16x16x128_f8f6f4 v[136:139], v[0:7], v[32:39], v[136:139]
	s_setprio 0
	s_barrier
	ds_read_b128 v[24:27], v207
	ds_read_b128 v[16:19], v207 offset:2048
	ds_read_b128 v[28:31], v208
	ds_read_b128 v[20:23], v208 offset:2048
	s_waitcnt vmcnt(8)
	s_and_b64 vcc, exec, s[0:1]
	s_cbranch_vccnz .LBB4_26
	s_mov_b32 m0, s36
	s_nop 0
	buffer_load_dwordx4 v193, s[48:51], 0 offen lds
	s_mov_b32 m0, s37
	s_nop 0
	buffer_load_dwordx4 v195, s[48:51], 0 offen lds
.LBB4_26:
	s_barrier
	s_waitcnt lgkmcnt(0)
	s_setprio 1
	v_mfma_f32_16x16x128_f8f6f4 v[180:183], v[24:31], v[56:63], v[180:183]
	s_and_b64 s[18:19], exec, s[18:19]
	s_cselect_b32 s12, s16, s12
	s_cselect_b32 s13, s9, s21
	v_mfma_f32_16x16x128_f8f6f4 v[176:179], v[16:23], v[56:63], v[176:179]
	s_add_u32 s12, s12, 0x80
	s_addc_u32 s13, s13, 0
	s_and_b32 s13, s13, 0xffff
	v_mfma_f32_16x16x128_f8f6f4 v[164:167], v[24:31], v[48:55], v[164:167]
	v_mfma_f32_16x16x128_f8f6f4 v[160:163], v[16:23], v[48:55], v[160:163]
	v_mfma_f32_16x16x128_f8f6f4 v[148:151], v[24:31], v[40:47], v[148:151]
	v_mfma_f32_16x16x128_f8f6f4 v[144:147], v[16:23], v[40:47], v[144:147]
	v_mfma_f32_16x16x128_f8f6f4 v[132:135], v[24:31], v[32:39], v[132:135]
	v_mfma_f32_16x16x128_f8f6f4 v[128:131], v[16:23], v[32:39], v[128:131]
	s_setprio 0
	s_barrier
	ds_read_b128 v[56:59], v200 offset:49152
	ds_read_b128 v[48:51], v200 offset:51200
	ds_read_b128 v[60:63], v201 offset:49152
	ds_read_b128 v[52:55], v201 offset:51200
	ds_read_b128 v[40:43], v200 offset:53248
	ds_read_b128 v[32:35], v200 offset:55296
	ds_read_b128 v[44:47], v201 offset:53248
	ds_read_b128 v[36:39], v201 offset:55296
	s_and_b64 vcc, exec, s[0:1]
	s_cbranch_vccnz .LBB4_28
	s_mov_b32 m0, s38
	s_nop 0
	buffer_load_dwordx4 v192, s[12:15], 0 offen lds
	s_mov_b32 m0, s39
	s_nop 0
	buffer_load_dwordx4 v194, s[12:15], 0 offen lds

.LBB5_18:
	ds_read_b128 v[0:3], v200
	ds_read_b128 v[8:11], v200 offset:2048
	ds_read_b128 v[4:7], v201
	ds_read_b128 v[12:15], v201 offset:2048
	s_mov_b32 m0, s43
	ds_read_b128 v[56:59], v198
	ds_read_b128 v[48:51], v198 offset:2048
	ds_read_b128 v[60:63], v199
	ds_read_b128 v[52:55], v199 offset:2048
	ds_read_b128 v[40:43], v198 offset:4096
	ds_read_b128 v[32:35], v198 offset:6144
	ds_read_b128 v[44:47], v199 offset:4096
	ds_read_b128 v[36:39], v199 offset:6144
	s_waitcnt vmcnt(8)
	buffer_load_dwordx4 v192, s[8:11], 0 offen lds
	s_mov_b32 m0, s44
	s_nop 0
	buffer_load_dwordx4 v193, s[8:11], 0 offen lds
	s_waitcnt lgkmcnt(8)
	s_barrier
	s_waitcnt lgkmcnt(0)
	s_setprio 1
	v_mfma_f32_16x16x128_f8f6f4 v[188:191], v[0:7], v[56:63], v[188:191]
	s_and_b32 s21, s49, 0xffff
	s_mov_b32 s22, s10
	s_mov_b32 s23, s11
	v_mfma_f32_16x16x128_f8f6f4 v[184:187], v[8:15], v[56:63], v[184:187]
	v_mfma_f32_16x16x128_f8f6f4 v[176:179], v[0:7], v[48:55], v[176:179]
	v_mfma_f32_16x16x128_f8f6f4 v[168:171], v[8:15], v[48:55], v[168:171]
	v_mfma_f32_16x16x128_f8f6f4 v[160:163], v[0:7], v[40:47], v[160:163]
	v_mfma_f32_16x16x128_f8f6f4 v[152:155], v[8:15], v[40:47], v[152:155]
	v_mfma_f32_16x16x128_f8f6f4 v[144:147], v[0:7], v[32:39], v[144:147]
	v_mfma_f32_16x16x128_f8f6f4 v[136:139], v[8:15], v[32:39], v[136:139]
	s_setprio 0
	s_barrier
	ds_read_b128 v[24:27], v202
	ds_read_b128 v[16:19], v202 offset:2048
	ds_read_b128 v[28:31], v203
	ds_read_b128 v[20:23], v203 offset:2048
	s_waitcnt vmcnt(8)
	s_and_b64 vcc, exec, s[18:19]
	s_cbranch_vccnz .LBB5_20
	s_mov_b32 m0, s29
	s_nop 0
	buffer_load_dwordx4 v192, s[20:23], 0 offen lds
	s_mov_b32 m0, s30
	s_nop 0
	buffer_load_dwordx4 v193, s[20:23], 0 offen lds
.LBB5_20:
	s_barrier
	s_waitcnt lgkmcnt(0)
	s_setprio 1
	v_mfma_f32_16x16x128_f8f6f4 v[180:183], v[24:31], v[56:63], v[180:183]
	s_add_u32 s8, s50, 0x100
	s_addc_u32 s21, s51, 0
	s_and_b32 s9, s21, 0xffff
	v_mfma_f32_16x16x128_f8f6f4 v[172:175], v[16:23], v[56:63], v[172:175]
	v_mfma_f32_16x16x128_f8f6f4 v[164:167], v[24:31], v[48:55], v[164:167]
	v_mfma_f32_16x16x128_f8f6f4 v[156:159], v[16:23], v[48:55], v[156:159]
	v_mfma_f32_16x16x128_f8f6f4 v[148:151], v[24:31], v[40:47], v[148:151]
	v_mfma_f32_16x16x128_f8f6f4 v[140:143], v[16:23], v[40:47], v[140:143]
	v_mfma_f32_16x16x128_f8f6f4 v[132:135], v[24:31], v[32:39], v[132:135]
	v_mfma_f32_16x16x128_f8f6f4 v[128:131], v[16:23], v[32:39], v[128:131]
	s_setprio 0
	s_barrier
	ds_read_b128 v[56:59], v198 offset:16384
	ds_read_b128 v[48:51], v198 offset:18432
	ds_read_b128 v[60:63], v199 offset:16384
	ds_read_b128 v[52:55], v199 offset:18432
	ds_read_b128 v[40:43], v198 offset:20480
	ds_read_b128 v[32:35], v198 offset:22528
	ds_read_b128 v[44:47], v199 offset:20480
	ds_read_b128 v[36:39], v199 offset:22528
	v_cndmask_b32_e64 v204, 0, 1, s[26:27]
	v_cmp_ne_u32_e64 s[0:1], 1, v204
	s_andn2_b64 vcc, exec, s[26:27]
	s_cbranch_vccnz .LBB5_22
	s_mov_b32 m0, s25
	s_nop 0
	buffer_load_dwordx4 v192, s[8:11], 0 offen lds
	s_mov_b32 m0, s31
	s_nop 0
	buffer_load_dwordx4 v193, s[8:11], 0 offen lds
.LBB5_22:
	s_barrier
	s_waitcnt lgkmcnt(0)
	s_setprio 1
	v_mfma_f32_16x16x128_f8f6f4 v[124:127], v[0:7], v[56:63], v[124:127]
	s_add_u32 s52, s47, 0x40100
	s_addc_u32 s9, s48, 0
	s_and_b32 s53, s9, 0xffff
	s_mov_b32 s54, s10
	v_mfma_f32_16x16x128_f8f6f4 v[120:123], v[8:15], v[56:63], v[120:123]
	s_mov_b32 s55, s11
	v_mfma_f32_16x16x128_f8f6f4 v[116:119], v[0:7], v[48:55], v[116:119]
	v_mfma_f32_16x16x128_f8f6f4 v[112:115], v[8:15], v[48:55], v[112:115]
	v_mfma_f32_16x16x128_f8f6f4 v[100:103], v[0:7], v[40:47], v[100:103]
	v_mfma_f32_16x16x128_f8f6f4 v[96:99], v[8:15], v[40:47], v[96:99]
	v_mfma_f32_16x16x128_f8f6f4 v[84:87], v[0:7], v[32:39], v[84:87]
	v_mfma_f32_16x16x128_f8f6f4 v[72:75], v[8:15], v[32:39], v[72:75]
	s_setprio 0
	s_barrier
	s_and_b64 vcc, exec, s[0:1]
	s_mov_b64 s[22:23], -1
	s_cbranch_vccnz .LBB5_24
	s_mov_b32 m0, s17
	s_nop 0
	buffer_load_dwordx4 v192, s[52:55], 0 offen lds
	s_mov_b32 m0, s33
	s_mov_b64 s[22:23], 0
	buffer_load_dwordx4 v193, s[52:55], 0 offen lds
	s_waitcnt vmcnt(10)

.LBB5_26:
	s_barrier
	s_setprio 1
	v_mfma_f32_16x16x128_f8f6f4 v[108:111], v[24:31], v[56:63], v[108:111]
	v_add_u32_e32 v0, s46, v196
	v_add_u32_e32 v4, s46, v197
	s_add_u32 s52, s50, 0x40100
	s_addc_u32 s9, s51, 0
	v_mfma_f32_16x16x128_f8f6f4 v[104:107], v[16:23], v[56:63], v[104:107]
	s_and_b32 s53, s9, 0xffff
	s_mov_b32 s54, s10
	s_mov_b32 s55, s11
	v_mfma_f32_16x16x128_f8f6f4 v[92:95], v[24:31], v[48:55], v[92:95]
	v_mfma_f32_16x16x128_f8f6f4 v[88:91], v[16:23], v[48:55], v[88:91]
	v_mfma_f32_16x16x128_f8f6f4 v[80:83], v[24:31], v[40:47], v[80:83]
	v_mfma_f32_16x16x128_f8f6f4 v[76:79], v[16:23], v[40:47], v[76:79]
	v_mfma_f32_16x16x128_f8f6f4 v[68:71], v[24:31], v[32:39], v[68:71]
	v_mfma_f32_16x16x128_f8f6f4 v[64:67], v[16:23], v[32:39], v[64:67]
	s_setprio 0
	s_barrier
	ds_read_b128 v[8:11], v0
	ds_read_b128 v[0:3], v0 offset:2048
	ds_read_b128 v[12:15], v4
	ds_read_b128 v[4:7], v4 offset:2048
	ds_read_b128 v[56:59], v198 offset:32768
	ds_read_b128 v[48:51], v198 offset:34816
	ds_read_b128 v[60:63], v199 offset:32768
	ds_read_b128 v[52:55], v199 offset:34816
	ds_read_b128 v[40:43], v198 offset:36864
	ds_read_b128 v[32:35], v198 offset:38912
	ds_read_b128 v[44:47], v199 offset:36864
	ds_read_b128 v[36:39], v199 offset:38912
	s_waitcnt vmcnt(8)
	s_and_b64 vcc, exec, s[0:1]
	s_cbranch_vccnz .LBB5_28
	s_mov_b32 m0, s34
	s_nop 0
	buffer_load_dwordx4 v192, s[52:55], 0 offen lds
	s_mov_b32 m0, s36
	s_nop 0
	buffer_load_dwordx4 v193, s[52:55], 0 offen lds
.LBB5_28:
	s_waitcnt lgkmcnt(8)
	s_barrier
	s_waitcnt lgkmcnt(0)
	s_setprio 1
	v_mfma_f32_16x16x128_f8f6f4 v[188:191], v[8:15], v[56:63], v[188:191]
	s_and_b64 s[22:23], exec, s[18:19]
	s_cselect_b32 s20, s12, s20
	s_cselect_b32 s9, s7, s49
	v_mfma_f32_16x16x128_f8f6f4 v[184:187], v[0:7], v[56:63], v[184:187]
	s_add_u32 s52, s20, 0x80
	s_addc_u32 s9, s9, 0
	s_and_b32 s53, s9, 0xffff
	s_mov_b32 s54, s10
	v_mfma_f32_16x16x128_f8f6f4 v[176:179], v[8:15], v[48:55], v[176:179]
	s_mov_b32 s55, s11
	v_mfma_f32_16x16x128_f8f6f4 v[168:171], v[0:7], v[48:55], v[168:171]
	v_mfma_f32_16x16x128_f8f6f4 v[160:163], v[8:15], v[40:47], v[160:163]
	v_mfma_f32_16x16x128_f8f6f4 v[152:155], v[0:7], v[40:47], v[152:155]
	v_mfma_f32_16x16x128_f8f6f4 v[144:147], v[8:15], v[32:39], v[144:147]
	v_mfma_f32_16x16x128_f8f6f4 v[136:139], v[0:7], v[32:39], v[136:139]
	s_setprio 0
	s_barrier
	ds_read_b128 v[24:27], v205
	ds_read_b128 v[16:19], v205 offset:2048
	ds_read_b128 v[28:31], v206
	ds_read_b128 v[20:23], v206 offset:2048
	s_waitcnt vmcnt(8)
	s_and_b64 vcc, exec, s[0:1]
	s_cbranch_vccnz .LBB5_30
	s_mov_b32 m0, s37
	s_nop 0
	buffer_load_dwordx4 v192, s[52:55], 0 offen lds
	s_mov_b32 m0, s38
	s_nop 0
	buffer_load_dwordx4 v193, s[52:55], 0 offen lds
.LBB5_30:
	s_barrier
	s_waitcnt lgkmcnt(0)
	s_setprio 1
	v_mfma_f32_16x16x128_f8f6f4 v[180:183], v[24:31], v[56:63], v[180:183]
	s_and_b64 s[18:19], exec, s[18:19]
	s_cselect_b32 s8, s16, s8
	s_cselect_b32 s9, s13, s21
	v_mfma_f32_16x16x128_f8f6f4 v[172:175], v[16:23], v[56:63], v[172:175]
	s_add_u32 s8, s8, 0x80
	s_addc_u32 s9, s9, 0
	s_and_b32 s9, s9, 0xffff
	v_mfma_f32_16x16x128_f8f6f4 v[164:167], v[24:31], v[48:55], v[164:167]
	v_mfma_f32_16x16x128_f8f6f4 v[156:159], v[16:23], v[48:55], v[156:159]
	v_mfma_f32_16x16x128_f8f6f4 v[148:151], v[24:31], v[40:47], v[148:151]
	v_mfma_f32_16x16x128_f8f6f4 v[140:143], v[16:23], v[40:47], v[140:143]
	v_mfma_f32_16x16x128_f8f6f4 v[132:135], v[24:31], v[32:39], v[132:135]
	v_mfma_f32_16x16x128_f8f6f4 v[128:131], v[16:23], v[32:39], v[128:131]
	s_setprio 0
	s_barrier
	ds_read_b128 v[56:59], v198 offset:49152
	ds_read_b128 v[48:51], v198 offset:51200
	ds_read_b128 v[60:63], v199 offset:49152
	ds_read_b128 v[52:55], v199 offset:51200
	ds_read_b128 v[40:43], v198 offset:53248
	ds_read_b128 v[32:35], v198 offset:55296
	ds_read_b128 v[44:47], v199 offset:53248
	ds_read_b128 v[36:39], v199 offset:55296
	s_and_b64 vcc, exec, s[0:1]
	s_cbranch_vccnz .LBB5_32
	s_mov_b32 m0, s39
	s_nop 0
	buffer_load_dwordx4 v192, s[8:11], 0 offen lds
	s_mov_b32 m0, s40
	s_nop 0
	buffer_load_dwordx4 v193, s[8:11], 0 offen lds
